# speedup vs baseline: 1.0116x; 1.0013x over previous
.LBB2_1:
	v_mfma_f32_32x32x16_f16 v[96:111], v[172:175], v[136:139], v[0:15]
	v_mfma_f32_32x32x16_f16 v[80:95], v[168:171], v[136:139], v[0:15]
	s_mov_b32 s17, s31
	s_mov_b32 s18, s15
	v_add_u32_e32 v185, s18, v181
	ds_read_b64_tr_b16 v[176:177], v185 offset:24576
	ds_read_b64_tr_b16 v[178:179], v185 offset:25088
	v_add_f32_e32 v116, v64, v65
	v_add_f32_e32 v116, v66, v116
	v_add_f32_e32 v116, v67, v116
	v_add_f32_e32 v116, v68, v116
	v_add_f32_e32 v116, v69, v116
	v_cvt_pk_f16_f32 v140, v64, v65
	v_cvt_pk_f16_f32 v141, v66, v67
	ds_read_b64_tr_b16 v[172:173], v185 offset:28672
	ds_read_b64_tr_b16 v[174:175], v185 offset:29184
	v_add_f32_e32 v64, v70, v116
	v_add_f32_e32 v64, v71, v64
	v_add_f32_e32 v64, v72, v64
	v_add_f32_e32 v64, v73, v64
	v_cvt_pk_f16_f32 v142, v68, v69
	v_cvt_pk_f16_f32 v143, v70, v71
	ds_read_b64_tr_b16 v[68:69], v185 offset:25600
	ds_read_b64_tr_b16 v[70:71], v185 offset:26112
	s_waitcnt lgkmcnt(11)
	v_mfma_f32_32x32x16_f16 v[96:111], v[164:167], v[128:131], v[96:111]
	v_add_f32_e32 v64, v74, v64
	v_add_f32_e32 v64, v75, v64
	v_add_f32_e32 v64, v76, v64
	v_add_f32_e32 v116, v77, v64
	v_cvt_pk_f16_f32 v132, v72, v73
	v_cvt_pk_f16_f32 v133, v74, v75
	ds_read_b64_tr_b16 v[64:65], v185 offset:29696
	ds_read_b64_tr_b16 v[66:67], v185 offset:30208
	s_waitcnt lgkmcnt(12)
	v_mfma_f32_32x32x16_f16 v[80:95], v[160:163], v[128:131], v[80:95]
	v_add_f32_e32 v72, v78, v116
	v_add_f32_e32 v72, v79, v72
	v_add_f32_e32 v72, v48, v72
	v_add_f32_e32 v116, v49, v72
	v_cvt_pk_f16_f32 v134, v76, v77
	v_cvt_pk_f16_f32 v135, v78, v79
	ds_read_b64_tr_b16 v[72:73], v185 offset:26624
	ds_read_b64_tr_b16 v[74:75], v185 offset:27136
	s_waitcnt lgkmcnt(13)
	v_mfma_f32_32x32x16_f16 v[96:111], v[156:159], v[120:123], v[96:111]
	v_add_f32_e32 v76, v50, v116
	v_add_f32_e32 v76, v51, v76
	v_add_f32_e32 v76, v52, v76
	v_add_f32_e32 v76, v53, v76
	v_cvt_pk_f16_f32 v124, v48, v49
	v_cvt_pk_f16_f32 v125, v50, v51
	ds_read_b64_tr_b16 v[48:49], v185 offset:30720
	ds_read_b64_tr_b16 v[50:51], v185 offset:31232
	s_waitcnt lgkmcnt(14)
	v_mfma_f32_32x32x16_f16 v[80:95], v[152:155], v[120:123], v[80:95]
	v_add_f32_e32 v76, v54, v76
	v_add_f32_e32 v76, v55, v76
	v_add_f32_e32 v76, v56, v76
	v_add_f32_e32 v76, v57, v76
	v_cvt_pk_f16_f32 v126, v52, v53
	v_cvt_pk_f16_f32 v127, v54, v55
	ds_read_b64_tr_b16 v[52:53], v185 offset:27648
	ds_read_b64_tr_b16 v[54:55], v185 offset:28160
	s_waitcnt lgkmcnt(14)
	v_mfma_f32_32x32x16_f16 v[96:111], v[148:151], v[112:115], v[96:111]
	v_add_f32_e32 v76, v58, v76
	v_add_f32_e32 v76, v59, v76
	v_add_f32_e32 v76, v60, v76
	v_add_f32_e32 v76, v61, v76
	v_cvt_pk_f16_f32 v116, v56, v57
	v_cvt_pk_f16_f32 v117, v58, v59
	ds_read_b64_tr_b16 v[56:57], v185 offset:31744
	ds_read_b64_tr_b16 v[58:59], v185 offset:32256
	v_mfma_f32_32x32x16_f16 v[80:95], v[144:147], v[112:115], v[80:95]
	v_add_f32_e32 v76, v62, v76
	v_add_f32_e32 v76, v63, v76
	v_cvt_pk_f16_f32 v118, v60, v61
	v_cvt_pk_f16_f32 v119, v62, v63
	s_add_i32 m0, s14, s25
	v_cmp_lt_f32_e32 vcc, s36, v76
	global_load_lds_dwordx4 v180, s[44:45]
	s_add_i32 m0, s28, s26
	s_add_u32 s44, s44, 0x2000
	global_load_lds_dwordx4 v180, s[46:47]
	s_addc_u32 s45, s45, 0
	s_add_u32 s46, s46, 0x2000
	s_addc_u32 s47, s47, 0
	s_cbranch_vccnz .Lmy_rare_1

.LBB2_4:
	v_mfma_f32_32x32x16_f16 v[64:79], v[60:63], v[136:139], v[0:15]
	v_mfma_f32_32x32x16_f16 v[48:63], v[148:151], v[136:139], v[0:15]
	v_add_u32_e32 v185, s17, v181
	ds_read_b64_tr_b16 v[144:145], v185 offset:24576
	ds_read_b64_tr_b16 v[146:147], v185 offset:25088
	v_add_f32_e32 v116, v96, v97
	v_add_f32_e32 v116, v98, v116
	v_add_f32_e32 v116, v99, v116
	v_add_f32_e32 v116, v100, v116
	v_add_f32_e32 v116, v101, v116
	v_cvt_pk_f16_f32 v140, v96, v97
	v_cvt_pk_f16_f32 v141, v98, v99
	ds_read_b64_tr_b16 v[152:153], v185 offset:28672
	ds_read_b64_tr_b16 v[154:155], v185 offset:29184
	v_add_f32_e32 v116, v102, v116
	v_add_f32_e32 v116, v103, v116
	v_add_f32_e32 v116, v104, v116
	v_add_f32_e32 v96, v105, v116
	v_cvt_pk_f16_f32 v142, v100, v101
	v_cvt_pk_f16_f32 v143, v102, v103
	ds_read_b64_tr_b16 v[148:149], v185 offset:25600
	ds_read_b64_tr_b16 v[150:151], v185 offset:26112
	s_waitcnt lgkmcnt(11)
	v_mfma_f32_32x32x16_f16 v[64:79], v[176:179], v[128:131], v[64:79]
	v_add_f32_e32 v96, v106, v96
	v_add_f32_e32 v96, v107, v96
	v_add_f32_e32 v96, v108, v96
	v_add_f32_e32 v96, v109, v96
	v_cvt_pk_f16_f32 v132, v104, v105
	v_cvt_pk_f16_f32 v133, v106, v107
	ds_read_b64_tr_b16 v[100:101], v185 offset:29696
	ds_read_b64_tr_b16 v[102:103], v185 offset:30208
	s_waitcnt lgkmcnt(12)
	v_mfma_f32_32x32x16_f16 v[48:63], v[172:175], v[128:131], v[48:63]
	v_add_f32_e32 v96, v110, v96
	v_add_f32_e32 v96, v111, v96
	v_add_f32_e32 v96, v80, v96
	v_add_f32_e32 v104, v81, v96
	v_cvt_pk_f16_f32 v134, v108, v109
	v_cvt_pk_f16_f32 v135, v110, v111
	ds_read_b64_tr_b16 v[96:97], v185 offset:26624
	ds_read_b64_tr_b16 v[98:99], v185 offset:27136
	s_waitcnt lgkmcnt(13)
	v_mfma_f32_32x32x16_f16 v[64:79], v[168:171], v[120:123], v[64:79]
	v_add_f32_e32 v104, v82, v104
	v_add_f32_e32 v104, v83, v104
	v_add_f32_e32 v104, v84, v104
	v_add_f32_e32 v104, v85, v104
	v_cvt_pk_f16_f32 v124, v80, v81
	v_cvt_pk_f16_f32 v125, v82, v83
	ds_read_b64_tr_b16 v[80:81], v185 offset:30720
	ds_read_b64_tr_b16 v[82:83], v185 offset:31232
	s_waitcnt lgkmcnt(14)
	v_mfma_f32_32x32x16_f16 v[48:63], v[164:167], v[120:123], v[48:63]
	v_add_f32_e32 v104, v86, v104
	v_add_f32_e32 v104, v87, v104
	v_add_f32_e32 v104, v88, v104
	v_add_f32_e32 v104, v89, v104
	v_cvt_pk_f16_f32 v126, v84, v85
	v_cvt_pk_f16_f32 v127, v86, v87
	ds_read_b64_tr_b16 v[84:85], v185 offset:27648
	ds_read_b64_tr_b16 v[86:87], v185 offset:28160
	s_waitcnt lgkmcnt(14)
	v_mfma_f32_32x32x16_f16 v[64:79], v[160:163], v[112:115], v[64:79]
	v_add_f32_e32 v104, v90, v104
	v_add_f32_e32 v104, v91, v104
	v_add_f32_e32 v104, v92, v104
	v_add_f32_e32 v104, v93, v104
	v_cvt_pk_f16_f32 v116, v88, v89
	v_cvt_pk_f16_f32 v117, v90, v91
	ds_read_b64_tr_b16 v[88:89], v185 offset:31744
	ds_read_b64_tr_b16 v[90:91], v185 offset:32256
	v_mfma_f32_32x32x16_f16 v[48:63], v[156:159], v[112:115], v[48:63]
	v_add_f32_e32 v104, v94, v104
	v_add_f32_e32 v104, v95, v104
	v_cvt_pk_f16_f32 v118, v92, v93
	v_cvt_pk_f16_f32 v119, v94, v95
	s_add_i32 m0, s19, s25
	v_cmp_lt_f32_e32 vcc, s36, v104
	global_load_lds_dwordx4 v180, s[44:45]
	s_add_i32 m0, s18, s26
	s_add_u32 s44, s44, 0x2000
	global_load_lds_dwordx4 v180, s[46:47]
	s_addc_u32 s45, s45, 0
	s_add_u32 s46, s46, 0x2000
	s_addc_u32 s47, s47, 0
	s_cbranch_vccnz .Lmy_rare_2
